# PEER static assignment: the last partial round (512 context tokens) is spread over all workgroups, 2 waves each, instead of 8 waves on 64 workgroups
# speedup vs baseline: 1.0178x; 1.0079x over previous
.LBB0_719:
	s_lshl_b32 s6, s33, 3
	s_add_i32 s6, s6, s88
	s_cmpk_lt_i32 s6, 0x4000
	s_cbranch_scc1 .Lpe_notail
	s_cmpk_lg_u32 s33, 0x100
	s_cbranch_scc1 .Lpe_notail
	s_and_b32 s8, s6, 7
	s_sub_i32 s9, s6, 0x4000
	s_lshr_b32 s9, s9, 3
	s_lshl_b32 s9, s9, 1
	s_add_i32 s9, s9, s8
	s_addk_i32 s9, 0x4000
	s_cmp_lt_u32 s8, 2
	s_cselect_b32 s6, s9, 0x7ffffff0
.Lpe_notail:
	v_mov_b32_e32 v247, s6
	s_ashr_i32 s89, s88, 31
	s_lshl_b64 s[74:75], s[88:89], 11
	s_lshl_b64 s[8:9], s[88:89], 2
	v_lshl_add_u64 v[24:25], v[128:129], 0, s[74:75]
	s_add_u32 s8, s37, s8
	global_load_dwordx4 v[20:23], v[24:25], off offset:1024
	s_addc_u32 s9, s73, s9
	global_load_dwordx4 v[24:27], v[24:25], off
	s_nop 0
	global_load_dword v248, v3, s[8:9]
	s_waitcnt vmcnt(6)
	v_lshlrev_b32_e32 v28, 16, v4
	v_cmp_lt_i32_e32 vcc, -1, v28
	v_lshlrev_b32_e32 v30, 16, v5
	v_lshlrev_b32_e32 v32, 16, v6
	v_cndmask_b32_e32 v29, v217, v218, vcc
	v_cmp_lt_i32_e32 vcc, -1, v4
	v_xor_b32_e32 v28, v29, v28
	v_lshlrev_b32_e32 v34, 16, v7
	v_cndmask_b32_e32 v29, v217, v218, vcc
	v_cmp_lt_i32_e32 vcc, -1, v30
	s_waitcnt vmcnt(3)
	v_lshlrev_b32_e32 v36, 16, v16
	v_lshlrev_b32_e32 v38, 16, v17
	v_cndmask_b32_e32 v31, v217, v218, vcc
	v_cmp_lt_i32_e32 vcc, -1, v5
	v_xor_b32_e32 v30, v31, v30
	v_lshlrev_b32_e32 v40, 16, v18
	v_cndmask_b32_e32 v31, v217, v218, vcc
	v_cmp_lt_i32_e32 vcc, -1, v32
	v_lshlrev_b32_e32 v42, 16, v19
	v_lshlrev_b32_e32 v44, 16, v12
	v_cndmask_b32_e32 v33, v217, v218, vcc
	v_cmp_lt_i32_e32 vcc, -1, v6
	v_xor_b32_e32 v32, v33, v32
	v_lshlrev_b32_e32 v46, 16, v13
	v_cndmask_b32_e32 v33, v217, v218, vcc
	v_cmp_lt_i32_e32 vcc, -1, v34
	v_lshlrev_b32_e32 v48, 16, v14
	v_lshlrev_b32_e32 v50, 16, v15
	v_cndmask_b32_e32 v35, v217, v218, vcc
	v_cmp_lt_i32_e32 vcc, -1, v7
	v_xor_b32_e32 v34, v35, v34
	v_lshlrev_b32_e32 v52, 16, v8
	v_cndmask_b32_e32 v35, v217, v218, vcc
	v_cmp_lt_i32_e32 vcc, -1, v36
	v_lshlrev_b32_e32 v54, 16, v9
	v_lshlrev_b32_e32 v56, 16, v10
	v_cndmask_b32_e32 v37, v217, v218, vcc
	v_cmp_lt_i32_e32 vcc, -1, v16
	v_xor_b32_e32 v36, v37, v36
	v_lshlrev_b32_e32 v58, 16, v11
	v_cndmask_b32_e32 v37, v217, v218, vcc
	v_cmp_lt_i32_e32 vcc, -1, v38
	v_bitop3_b32 v29, v29, v4, s90 bitop3:0x78
	v_bitop3_b32 v31, v31, v5, s90 bitop3:0x78
	v_cndmask_b32_e32 v39, v217, v218, vcc
	v_cmp_lt_i32_e32 vcc, -1, v17
	v_xor_b32_e32 v38, v39, v38
	v_bitop3_b32 v33, v33, v6, s90 bitop3:0x78
	v_cndmask_b32_e32 v39, v217, v218, vcc
	v_cmp_lt_i32_e32 vcc, -1, v40
	v_bitop3_b32 v35, v35, v7, s90 bitop3:0x78
	v_bitop3_b32 v37, v37, v16, s90 bitop3:0x78
	v_cndmask_b32_e32 v41, v217, v218, vcc
	v_cmp_lt_i32_e32 vcc, -1, v18
	v_xor_b32_e32 v40, v41, v40
	v_bitop3_b32 v39, v39, v17, s90 bitop3:0x78
	v_cndmask_b32_e32 v41, v217, v218, vcc
	v_cmp_lt_i32_e32 vcc, -1, v42
	v_bitop3_b32 v41, v41, v18, s90 bitop3:0x78
	v_sub_u32_e32 v28, v28, v201
	v_cndmask_b32_e32 v43, v217, v218, vcc
	v_cmp_lt_i32_e32 vcc, -1, v19
	v_xor_b32_e32 v42, v43, v42
	v_sub_u32_e32 v29, v29, v201
	v_cndmask_b32_e32 v43, v217, v218, vcc
	v_cmp_lt_i32_e32 vcc, -1, v44
	v_bitop3_b32 v43, v43, v19, s90 bitop3:0x78
	v_sub_u32_e32 v30, v30, v202
	v_cndmask_b32_e32 v45, v217, v218, vcc
	v_cmp_lt_i32_e32 vcc, -1, v12
	v_xor_b32_e32 v44, v45, v44
	v_sub_u32_e32 v31, v31, v202
	v_cndmask_b32_e32 v45, v217, v218, vcc
	v_cmp_lt_i32_e32 vcc, -1, v46
	v_bitop3_b32 v45, v45, v12, s90 bitop3:0x78
	v_sub_u32_e32 v32, v32, v203
	v_cndmask_b32_e32 v47, v217, v218, vcc
	v_cmp_lt_i32_e32 vcc, -1, v13
	v_xor_b32_e32 v46, v47, v46
	v_sub_u32_e32 v33, v33, v203
	v_cndmask_b32_e32 v47, v217, v218, vcc
	v_cmp_lt_i32_e32 vcc, -1, v48
	v_bitop3_b32 v47, v47, v13, s90 bitop3:0x78
	v_sub_u32_e32 v34, v34, v204
	v_cndmask_b32_e32 v49, v217, v218, vcc
	v_cmp_lt_i32_e32 vcc, -1, v14
	v_xor_b32_e32 v48, v49, v48
	v_sub_u32_e32 v35, v35, v204
	v_cndmask_b32_e32 v49, v217, v218, vcc
	v_cmp_lt_i32_e32 vcc, -1, v50
	v_bitop3_b32 v49, v49, v14, s90 bitop3:0x78
	v_sub_u32_e32 v36, v36, v205
	v_cndmask_b32_e32 v51, v217, v218, vcc
	v_cmp_lt_i32_e32 vcc, -1, v15
	v_xor_b32_e32 v50, v51, v50
	v_sub_u32_e32 v37, v37, v205
	v_cndmask_b32_e32 v51, v217, v218, vcc
	v_cmp_lt_i32_e32 vcc, -1, v52
	v_bitop3_b32 v51, v51, v15, s90 bitop3:0x78
	v_sub_u32_e32 v38, v38, v220
	v_cndmask_b32_e32 v53, v217, v218, vcc
	v_cmp_lt_i32_e32 vcc, -1, v8
	v_xor_b32_e32 v52, v53, v52
	v_sub_u32_e32 v39, v39, v220
	v_cndmask_b32_e32 v53, v217, v218, vcc
	v_cmp_lt_i32_e32 vcc, -1, v54
	v_bitop3_b32 v53, v53, v8, s90 bitop3:0x78
	v_sub_u32_e32 v40, v40, v221
	v_cndmask_b32_e32 v55, v217, v218, vcc
	v_cmp_lt_i32_e32 vcc, -1, v9
	v_xor_b32_e32 v54, v55, v54
	v_sub_u32_e32 v41, v41, v221
	v_cndmask_b32_e32 v55, v217, v218, vcc
	v_cmp_lt_i32_e32 vcc, -1, v56
	v_bitop3_b32 v55, v55, v9, s90 bitop3:0x78
	v_sub_u32_e32 v42, v42, v222
	v_cndmask_b32_e32 v57, v217, v218, vcc
	v_cmp_lt_i32_e32 vcc, -1, v10
	v_xor_b32_e32 v56, v57, v56
	v_sub_u32_e32 v43, v43, v222
	v_cndmask_b32_e32 v57, v217, v218, vcc
	v_cmp_lt_i32_e32 vcc, -1, v58
	v_bitop3_b32 v57, v57, v10, s90 bitop3:0x78
	v_sub_u32_e32 v44, v44, v223
	v_cndmask_b32_e32 v59, v217, v218, vcc
	v_cmp_lt_i32_e32 vcc, -1, v11
	v_xor_b32_e32 v58, v59, v58
	v_sub_u32_e32 v45, v45, v223
	v_cndmask_b32_e32 v59, v217, v218, vcc
	v_bitop3_b32 v59, v59, v11, s90 bitop3:0x78
	v_sub_u32_e32 v46, v46, v224
	v_sub_u32_e32 v47, v47, v224
	v_sub_u32_e32 v48, v48, v225
	v_sub_u32_e32 v49, v49, v225
	v_sub_u32_e32 v50, v50, v226
	v_sub_u32_e32 v51, v51, v226
	v_sub_u32_e32 v52, v52, v227
	v_sub_u32_e32 v53, v53, v227
	v_sub_u32_e32 v54, v54, v228
	v_sub_u32_e32 v55, v55, v228
	v_sub_u32_e32 v56, v56, v229
	v_sub_u32_e32 v57, v57, v229
	v_sub_u32_e32 v58, v58, v230
	v_sub_u32_e32 v59, v59, v230
	v_add_u32_e32 v28, 0x7f, v28
	v_add_u32_e32 v29, 0x7e, v29
	v_add_u32_e32 v30, 0x7f, v30
	v_add_u32_e32 v31, 0x7e, v31
	v_add_u32_e32 v32, 0x7f, v32
	v_add_u32_e32 v33, 0x7e, v33
	v_add_u32_e32 v34, 0x7f, v34
	v_add_u32_e32 v35, 0x7e, v35
	v_add_u32_e32 v36, 0x7f, v36
	v_add_u32_e32 v37, 0x7e, v37
	v_add_u32_e32 v38, 0x7f, v38
	v_add_u32_e32 v39, 0x7e, v39
	v_add_u32_e32 v40, 0x7f, v40
	v_add_u32_e32 v41, 0x7e, v41
	v_add_u32_e32 v42, 0x7f, v42
	v_add_u32_e32 v43, 0x7e, v43
	v_add_u32_e32 v44, 0x7f, v44
	v_add_u32_e32 v45, 0x7e, v45
	v_add_u32_e32 v46, 0x7f, v46
	v_add_u32_e32 v47, 0x7e, v47
	v_add_u32_e32 v48, 0x7f, v48
	v_add_u32_e32 v49, 0x7e, v49
	v_add_u32_e32 v50, 0x7f, v50
	v_add_u32_e32 v51, 0x7e, v51
	v_add_u32_e32 v52, 0x7f, v52
	v_add_u32_e32 v53, 0x7e, v53
	v_add_u32_e32 v54, 0x7f, v54
	v_add_u32_e32 v55, 0x7e, v55
	v_add_u32_e32 v56, 0x7f, v56
	v_add_u32_e32 v57, 0x7e, v57
	v_add_u32_e32 v58, 0x7f, v58
	v_add_u32_e32 v59, 0x7e, v59
	v_max_u32_e32 v60, v28, v29
	v_min_u32_e32 v28, v28, v29
	v_max_u32_e32 v29, v30, v31
	v_min_u32_e32 v30, v30, v31
	v_max_u32_e32 v31, v32, v33
	v_min_u32_e32 v32, v32, v33
	v_max_u32_e32 v33, v34, v35
	v_min_u32_e32 v34, v34, v35
	v_max_u32_e32 v35, v36, v37
	v_min_u32_e32 v36, v36, v37
	v_max_u32_e32 v37, v38, v39
	v_min_u32_e32 v38, v38, v39
	v_max_u32_e32 v39, v40, v41
	v_min_u32_e32 v40, v40, v41
	v_max_u32_e32 v41, v42, v43
	v_min_u32_e32 v42, v42, v43
	v_max_u32_e32 v43, v44, v45
	v_min_u32_e32 v44, v44, v45
	v_max_u32_e32 v45, v46, v47
	v_min_u32_e32 v46, v46, v47
	v_max_u32_e32 v47, v48, v49
	v_min_u32_e32 v48, v48, v49
	v_max_u32_e32 v49, v50, v51
	v_min_u32_e32 v50, v50, v51
	v_max_u32_e32 v51, v52, v53
	v_min_u32_e32 v52, v52, v53
	v_max_u32_e32 v53, v54, v55
	v_min_u32_e32 v54, v54, v55
	v_max_u32_e32 v55, v56, v57
	v_min_u32_e32 v56, v56, v57
	v_max_u32_e32 v57, v58, v59
	v_min_u32_e32 v58, v58, v59
	v_max_u32_e32 v59, v60, v30
	v_min_u32_e32 v30, v60, v30
	v_max_u32_e32 v60, v28, v29
	v_min_u32_e32 v28, v28, v29
	v_max_u32_e32 v29, v31, v34
	v_min_u32_e32 v31, v31, v34
	v_max_u32_e32 v34, v32, v33
	v_min_u32_e32 v32, v32, v33
	v_max_u32_e32 v33, v35, v38
	v_min_u32_e32 v35, v35, v38
	v_max_u32_e32 v38, v36, v37
	v_min_u32_e32 v36, v36, v37
	v_max_u32_e32 v37, v39, v42
	v_min_u32_e32 v39, v39, v42
	v_max_u32_e32 v42, v40, v41
	v_min_u32_e32 v40, v40, v41
	v_max_u32_e32 v41, v43, v46
	v_min_u32_e32 v43, v43, v46
	v_max_u32_e32 v46, v44, v45
	v_min_u32_e32 v44, v44, v45
	v_max_u32_e32 v45, v47, v50
	v_min_u32_e32 v47, v47, v50
	v_max_u32_e32 v50, v48, v49
	v_min_u32_e32 v48, v48, v49
	v_max_u32_e32 v49, v51, v54
	v_min_u32_e32 v51, v51, v54
	v_max_u32_e32 v54, v52, v53
	v_min_u32_e32 v52, v52, v53
	v_max_u32_e32 v53, v55, v58
	v_min_u32_e32 v55, v55, v58
	v_max_u32_e32 v58, v56, v57
	v_min_u32_e32 v56, v56, v57
	v_max_u32_e32 v57, v59, v60
	v_min_u32_e32 v59, v59, v60
	v_max_u32_e32 v60, v30, v28
	v_min_u32_e32 v28, v30, v28
	v_max_u32_e32 v30, v31, v32
	v_min_u32_e32 v31, v31, v32
	v_max_u32_e32 v32, v29, v34
	v_min_u32_e32 v29, v29, v34
	v_max_u32_e32 v34, v33, v38
	v_min_u32_e32 v33, v33, v38
	v_max_u32_e32 v38, v35, v36
	v_min_u32_e32 v35, v35, v36
	v_max_u32_e32 v36, v39, v40
	v_min_u32_e32 v39, v39, v40
	v_max_u32_e32 v40, v37, v42
	v_min_u32_e32 v37, v37, v42
	v_max_u32_e32 v42, v41, v46
	v_min_u32_e32 v41, v41, v46
	v_max_u32_e32 v46, v43, v44
	v_min_u32_e32 v43, v43, v44
	v_max_u32_e32 v44, v47, v48
	v_min_u32_e32 v47, v47, v48
	v_max_u32_e32 v48, v45, v50
	v_min_u32_e32 v45, v45, v50
	v_max_u32_e32 v50, v49, v54
	v_min_u32_e32 v49, v49, v54
	v_max_u32_e32 v54, v51, v52
	v_min_u32_e32 v51, v51, v52
	v_max_u32_e32 v52, v55, v56
	v_min_u32_e32 v55, v55, v56
	v_max_u32_e32 v56, v53, v58
	v_min_u32_e32 v53, v53, v58
	v_max_u32_e32 v58, v57, v31
	v_min_u32_e32 v31, v57, v31
	v_max_u32_e32 v57, v59, v30
	v_min_u32_e32 v30, v59, v30
	v_max_u32_e32 v59, v60, v29
	v_min_u32_e32 v29, v60, v29
	v_max_u32_e32 v60, v28, v32
	v_min_u32_e32 v28, v28, v32
	v_max_u32_e32 v32, v34, v39
	v_min_u32_e32 v34, v34, v39
	v_max_u32_e32 v39, v33, v36
	v_min_u32_e32 v33, v33, v36
	v_max_u32_e32 v36, v38, v37
	v_min_u32_e32 v37, v38, v37
	v_max_u32_e32 v38, v35, v40
	v_min_u32_e32 v35, v35, v40
	v_max_u32_e32 v40, v42, v47
	v_min_u32_e32 v42, v42, v47
	v_max_u32_e32 v47, v41, v44
	v_min_u32_e32 v41, v41, v44
	v_max_u32_e32 v44, v46, v45
	v_min_u32_e32 v45, v46, v45
	v_max_u32_e32 v46, v43, v48
	v_min_u32_e32 v43, v43, v48
	v_max_u32_e32 v48, v50, v55
	v_min_u32_e32 v50, v50, v55
	v_max_u32_e32 v55, v49, v52
	v_min_u32_e32 v49, v49, v52
	v_max_u32_e32 v52, v54, v53
	v_min_u32_e32 v53, v54, v53
	v_max_u32_e32 v54, v51, v56
	v_min_u32_e32 v51, v51, v56
	v_max_u32_e32 v56, v58, v59
	v_min_u32_e32 v58, v58, v59
	v_max_u32_e32 v59, v57, v60
	v_min_u32_e32 v57, v57, v60
	v_max_u32_e32 v60, v31, v29
	v_min_u32_e32 v29, v31, v29
	v_max_u32_e32 v31, v30, v28
	v_min_u32_e32 v28, v30, v28
	v_max_u32_e32 v30, v34, v37
	v_min_u32_e32 v34, v34, v37
	v_max_u32_e32 v37, v33, v35
	v_min_u32_e32 v33, v33, v35
	v_max_u32_e32 v35, v32, v36
	v_min_u32_e32 v32, v32, v36
	v_max_u32_e32 v36, v39, v38
	v_min_u32_e32 v38, v39, v38
	v_max_u32_e32 v39, v40, v44
	v_min_u32_e32 v40, v40, v44
	v_max_u32_e32 v44, v47, v46
	v_min_u32_e32 v46, v47, v46
	v_max_u32_e32 v47, v42, v45
	v_min_u32_e32 v42, v42, v45
	v_max_u32_e32 v45, v41, v43
	v_min_u32_e32 v41, v41, v43
	v_max_u32_e32 v43, v50, v53
	v_min_u32_e32 v50, v50, v53
	v_max_u32_e32 v53, v49, v51
	v_min_u32_e32 v49, v49, v51
	v_max_u32_e32 v51, v48, v52
	v_min_u32_e32 v48, v48, v52
	v_max_u32_e32 v52, v55, v54
	v_min_u32_e32 v54, v55, v54
	v_max_u32_e32 v55, v56, v59
	v_min_u32_e32 v56, v56, v59
	v_max_u32_e32 v59, v58, v57
	v_min_u32_e32 v57, v58, v57
	v_max_u32_e32 v58, v60, v31
	v_min_u32_e32 v31, v60, v31
	v_max_u32_e32 v60, v29, v28
	v_min_u32_e32 v28, v29, v28
	v_max_u32_e32 v29, v34, v33
	v_min_u32_e32 v33, v34, v33
	v_max_u32_e32 v34, v30, v37
	v_min_u32_e32 v30, v30, v37
	v_max_u32_e32 v37, v32, v38
	v_min_u32_e32 v32, v32, v38
	v_max_u32_e32 v38, v35, v36
	v_min_u32_e32 v35, v35, v36
	v_max_u32_e32 v36, v39, v44
	v_min_u32_e32 v39, v39, v44
	v_max_u32_e32 v44, v40, v46
	v_min_u32_e32 v40, v40, v46
	v_max_u32_e32 v46, v47, v45
	v_min_u32_e32 v45, v47, v45
	v_max_u32_e32 v47, v42, v41
	v_min_u32_e32 v41, v42, v41
	v_max_u32_e32 v42, v50, v49
	v_min_u32_e32 v49, v50, v49
	v_max_u32_e32 v50, v43, v53
	v_min_u32_e32 v43, v43, v53
	v_max_u32_e32 v53, v48, v54
	v_min_u32_e32 v48, v48, v54
	v_max_u32_e32 v54, v51, v52
	v_min_u32_e32 v51, v51, v52
	v_max_u32_e32 v52, v55, v33
	v_min_u32_e32 v33, v55, v33
	v_max_u32_e32 v55, v56, v29
	v_min_u32_e32 v29, v56, v29
	v_max_u32_e32 v56, v59, v30
	v_min_u32_e32 v30, v59, v30
	v_max_u32_e32 v59, v57, v34
	v_min_u32_e32 v34, v57, v34
	v_max_u32_e32 v57, v58, v32
	v_min_u32_e32 v32, v58, v32
	v_max_u32_e32 v58, v31, v37
	v_min_u32_e32 v31, v31, v37
	v_max_u32_e32 v37, v60, v35
	v_min_u32_e32 v35, v60, v35
	v_max_u32_e32 v60, v28, v38
	v_min_u32_e32 v28, v28, v38
	v_max_u32_e32 v38, v36, v49
	v_min_u32_e32 v36, v36, v49
	v_max_u32_e32 v49, v39, v42
	v_min_u32_e32 v39, v39, v42
	v_max_u32_e32 v42, v44, v43
	v_min_u32_e32 v43, v44, v43
	v_max_u32_e32 v44, v40, v50
	v_min_u32_e32 v40, v40, v50
	v_max_u32_e32 v50, v46, v48
	v_min_u32_e32 v46, v46, v48
	v_max_u32_e32 v48, v45, v53
	v_min_u32_e32 v45, v45, v53
	v_max_u32_e32 v53, v47, v51
	v_min_u32_e32 v47, v47, v51
	v_max_u32_e32 v51, v41, v54
	v_min_u32_e32 v41, v41, v54
	v_max_u32_e32 v54, v52, v57
	v_min_u32_e32 v52, v52, v57
	v_max_u32_e32 v57, v55, v58
	v_min_u32_e32 v55, v55, v58
	v_max_u32_e32 v58, v56, v37
	v_min_u32_e32 v37, v56, v37
	v_max_u32_e32 v56, v59, v60
	v_min_u32_e32 v59, v59, v60
	v_max_u32_e32 v60, v33, v32
	v_min_u32_e32 v32, v33, v32
	v_max_u32_e32 v33, v29, v31
	v_min_u32_e32 v29, v29, v31
	v_max_u32_e32 v31, v30, v35
	v_min_u32_e32 v30, v30, v35
	v_max_u32_e32 v35, v34, v28
	v_min_u32_e32 v28, v34, v28
	v_max_u32_e32 v34, v36, v46
	v_min_u32_e32 v36, v36, v46
	v_max_u32_e32 v46, v39, v45
	v_min_u32_e32 v39, v39, v45
	v_max_u32_e32 v45, v43, v47
	v_min_u32_e32 v43, v43, v47
	v_max_u32_e32 v47, v40, v41
	v_min_u32_e32 v40, v40, v41
	v_max_u32_e32 v41, v38, v50
	v_min_u32_e32 v38, v38, v50
	v_max_u32_e32 v50, v49, v48
	v_min_u32_e32 v48, v49, v48
	v_max_u32_e32 v49, v42, v53
	v_min_u32_e32 v42, v42, v53
	v_max_u32_e32 v53, v44, v51
	v_min_u32_e32 v44, v44, v51
	v_max_u32_e32 v51, v54, v58
	v_min_u32_e32 v54, v54, v58
	v_max_u32_e32 v58, v57, v56
	v_min_u32_e32 v56, v57, v56
	v_max_u32_e32 v57, v52, v37
	v_min_u32_e32 v37, v52, v37
	v_max_u32_e32 v52, v55, v59
	v_min_u32_e32 v55, v55, v59
	v_max_u32_e32 v59, v60, v31
	v_min_u32_e32 v31, v60, v31
	v_max_u32_e32 v60, v33, v35
	v_min_u32_e32 v33, v33, v35
	v_max_u32_e32 v35, v32, v30
	v_min_u32_e32 v30, v32, v30
	v_max_u32_e32 v32, v29, v28
	v_min_u32_e32 v28, v29, v28
	v_max_u32_e32 v29, v36, v43
	v_min_u32_e32 v36, v36, v43
	v_max_u32_e32 v43, v39, v40
	v_min_u32_e32 v39, v39, v40
	v_max_u32_e32 v40, v34, v45
	v_min_u32_e32 v34, v34, v45
	v_max_u32_e32 v45, v46, v47
	v_min_u32_e32 v46, v46, v47
	v_max_u32_e32 v47, v38, v42
	v_min_u32_e32 v38, v38, v42
	v_max_u32_e32 v42, v48, v44
	v_min_u32_e32 v44, v48, v44
	v_max_u32_e32 v48, v41, v49
	v_min_u32_e32 v41, v41, v49
	v_max_u32_e32 v49, v50, v53
	v_min_u32_e32 v50, v50, v53
	v_min_u32_e32 v53, v51, v58
	v_min_u32_e32 v61, v54, v56
	v_min_u32_e32 v62, v57, v52
	v_min_u32_e32 v63, v37, v55
	v_min_u32_e32 v64, v59, v60
	v_min_u32_e32 v65, v31, v33
	v_min_u32_e32 v66, v35, v32
	v_min_u32_e32 v67, v30, v28
	v_min_u32_e32 v68, v36, v39
	v_min_u32_e32 v69, v29, v43
	v_min_u32_e32 v70, v34, v46
	v_min_u32_e32 v71, v40, v45
	v_min_u32_e32 v72, v38, v44
	v_min_u32_e32 v73, v47, v42
	v_min_u32_e32 v74, v41, v50
	v_min_u32_e32 v75, v48, v49
	v_max3_u32 v51, v51, v58, v68
	v_max3_u32 v36, v53, v36, v39
	v_max3_u32 v39, v54, v56, v69
	v_max3_u32 v29, v61, v29, v43
	v_max3_u32 v43, v57, v52, v70
	v_max3_u32 v34, v62, v34, v46
	v_max3_u32 v37, v37, v55, v71
	v_max3_u32 v40, v63, v40, v45
	v_max3_u32 v45, v59, v60, v72
	v_max3_u32 v38, v64, v38, v44
	v_max3_u32 v31, v31, v33, v73
	v_max3_u32 v33, v65, v47, v42
	v_max3_u32 v32, v35, v32, v74
	v_max3_u32 v35, v66, v41, v50
	v_max3_u32 v28, v30, v28, v75
	v_max3_u32 v30, v67, v48, v49
	v_max_u32_e32 v41, v51, v45
	v_min_u32_e32 v42, v51, v45
	v_max_u32_e32 v44, v36, v38
	v_min_u32_e32 v36, v36, v38
	v_max_u32_e32 v38, v39, v31
	v_min_u32_e32 v31, v39, v31
	v_max_u32_e32 v39, v29, v33
	v_min_u32_e32 v29, v29, v33
	v_max_u32_e32 v33, v43, v32
	v_min_u32_e32 v32, v43, v32
	v_max_u32_e32 v43, v34, v35
	v_min_u32_e32 v34, v34, v35
	v_max_u32_e32 v35, v37, v28
	v_min_u32_e32 v28, v37, v28
	v_max_u32_e32 v37, v40, v30
	v_min_u32_e32 v30, v40, v30
	v_max_u32_e32 v40, v41, v33
	v_min_u32_e32 v33, v41, v33
	v_max_u32_e32 v41, v44, v43
	v_min_u32_e32 v43, v44, v43
	v_max_u32_e32 v44, v38, v35
	v_min_u32_e32 v35, v38, v35
	v_max_u32_e32 v38, v39, v37
	v_min_u32_e32 v37, v39, v37
	v_max_u32_e32 v39, v42, v32
	v_min_u32_e32 v32, v42, v32
	v_max_u32_e32 v42, v36, v34
	v_min_u32_e32 v34, v36, v34
	v_max_u32_e32 v36, v31, v28
	v_min_u32_e32 v28, v31, v28
	v_max_u32_e32 v31, v29, v30
	v_min_u32_e32 v29, v29, v30
	v_max_u32_e32 v30, v40, v44
	v_min_u32_e32 v40, v40, v44
	v_max_u32_e32 v44, v41, v38
	v_min_u32_e32 v38, v41, v38
	v_max_u32_e32 v41, v33, v35
	v_min_u32_e32 v33, v33, v35
	v_max_u32_e32 v35, v43, v37
	v_min_u32_e32 v37, v43, v37
	v_max_u32_e32 v43, v39, v36
	v_min_u32_e32 v36, v39, v36
	v_max_u32_e32 v39, v42, v31
	v_min_u32_e32 v31, v42, v31
	v_max_u32_e32 v42, v32, v28
	v_min_u32_e32 v28, v32, v28
	v_max_u32_e32 v32, v34, v29
	v_min_u32_e32 v29, v34, v29
	v_max_u32_e32 v34, v30, v44
	v_min_u32_e32 v30, v30, v44
	v_max_u32_e32 v44, v40, v38
	v_min_u32_e32 v38, v40, v38
	v_max_u32_e32 v40, v41, v35
	v_min_u32_e32 v35, v41, v35
	v_max_u32_e32 v41, v33, v37
	v_min_u32_e32 v33, v33, v37
	v_max_u32_e32 v37, v43, v39
	v_min_u32_e32 v39, v43, v39
	v_max_u32_e32 v43, v36, v31
	v_min_u32_e32 v31, v36, v31
	v_max_u32_e32 v36, v42, v32
	v_min_u32_e32 v32, v42, v32
	v_max_u32_e32 v42, v28, v29
	v_min_u32_e32 v28, v28, v29
	v_max_u32_dpp v46, v32, v44 quad_perm:[1,0,3,2] row_mask:0xf bank_mask:0xf bound_ctrl:1
	v_max_u32_dpp v45, v42, v30 quad_perm:[1,0,3,2] row_mask:0xf bank_mask:0xf bound_ctrl:1
	v_max_u32_dpp v29, v28, v34 quad_perm:[1,0,3,2] row_mask:0xf bank_mask:0xf bound_ctrl:1
	v_max_u32_dpp v47, v36, v38 quad_perm:[1,0,3,2] row_mask:0xf bank_mask:0xf bound_ctrl:1
	v_max_u32_dpp v48, v31, v40 quad_perm:[1,0,3,2] row_mask:0xf bank_mask:0xf bound_ctrl:1
	v_max_u32_dpp v49, v43, v35 quad_perm:[1,0,3,2] row_mask:0xf bank_mask:0xf bound_ctrl:1
	v_max_u32_dpp v50, v39, v41 quad_perm:[1,0,3,2] row_mask:0xf bank_mask:0xf bound_ctrl:1
	v_max_u32_dpp v51, v37, v33 quad_perm:[1,0,3,2] row_mask:0xf bank_mask:0xf bound_ctrl:1
	v_max_u32_dpp v33, v33, v37 quad_perm:[1,0,3,2] row_mask:0xf bank_mask:0xf bound_ctrl:1
	v_max_u32_dpp v37, v41, v39 quad_perm:[1,0,3,2] row_mask:0xf bank_mask:0xf bound_ctrl:1
	v_max_u32_dpp v35, v35, v43 quad_perm:[1,0,3,2] row_mask:0xf bank_mask:0xf bound_ctrl:1
	v_max_u32_dpp v31, v40, v31 quad_perm:[1,0,3,2] row_mask:0xf bank_mask:0xf bound_ctrl:1
	v_max_u32_dpp v36, v38, v36 quad_perm:[1,0,3,2] row_mask:0xf bank_mask:0xf bound_ctrl:1
	v_max_u32_dpp v32, v44, v32 quad_perm:[1,0,3,2] row_mask:0xf bank_mask:0xf bound_ctrl:1
	v_max_u32_dpp v30, v30, v42 quad_perm:[1,0,3,2] row_mask:0xf bank_mask:0xf bound_ctrl:1
	v_max_u32_dpp v28, v34, v28 quad_perm:[1,0,3,2] row_mask:0xf bank_mask:0xf bound_ctrl:1
	v_max_u32_e32 v34, v29, v33
	v_min_u32_e32 v29, v29, v33
	v_max_u32_e32 v33, v45, v37
	v_min_u32_e32 v37, v45, v37
	v_max_u32_e32 v38, v46, v35
	v_min_u32_e32 v35, v46, v35
	v_max_u32_e32 v39, v47, v31
	v_min_u32_e32 v31, v47, v31
	v_max_u32_e32 v40, v48, v36
	v_min_u32_e32 v36, v48, v36
	v_max_u32_e32 v41, v49, v32
	v_min_u32_e32 v32, v49, v32
	v_max_u32_e32 v42, v50, v30
	v_min_u32_e32 v30, v50, v30
	v_max_u32_e32 v43, v51, v28
	v_min_u32_e32 v28, v51, v28
	v_max_u32_e32 v44, v34, v40
	v_min_u32_e32 v34, v34, v40
	v_max_u32_e32 v40, v33, v41
	v_min_u32_e32 v33, v33, v41
	v_max_u32_e32 v41, v38, v42
	v_min_u32_e32 v38, v38, v42
	v_max_u32_e32 v42, v39, v43
	v_min_u32_e32 v39, v39, v43
	v_max_u32_e32 v43, v29, v36
	v_min_u32_e32 v29, v29, v36
	v_max_u32_e32 v36, v37, v32
	v_min_u32_e32 v32, v37, v32
	v_max_u32_e32 v37, v35, v30
	v_min_u32_e32 v30, v35, v30
	v_max_u32_e32 v35, v31, v28
	v_min_u32_e32 v28, v31, v28
	v_max_u32_e32 v31, v44, v41
	v_min_u32_e32 v41, v44, v41
	v_max_u32_e32 v44, v40, v42
	v_min_u32_e32 v42, v40, v42
	v_max_u32_e32 v45, v34, v38
	v_min_u32_e32 v34, v34, v38
	v_max_u32_e32 v38, v33, v39
	v_min_u32_e32 v33, v33, v39
	v_max_u32_e32 v39, v43, v37
	v_min_u32_e32 v43, v43, v37
	v_max_u32_e32 v46, v36, v35
	v_min_u32_e32 v35, v36, v35
	v_max_u32_e32 v47, v29, v30
	v_min_u32_e32 v50, v29, v30
	v_max_u32_e32 v51, v32, v28
	v_min_u32_e32 v52, v32, v28
	v_max_u32_e32 v40, v31, v44
	v_min_u32_e32 v30, v31, v44
	v_max_u32_e32 v36, v41, v42
	v_min_u32_e32 v28, v41, v42
	v_max_u32_e32 v41, v45, v38
	v_min_u32_e32 v31, v45, v38
	v_max_u32_e32 v37, v34, v33
	v_min_u32_e32 v29, v34, v33
	v_max_u32_e32 v48, v39, v46
	v_min_u32_e32 v34, v39, v46
	v_max_u32_e32 v42, v43, v35
	v_min_u32_e32 v32, v43, v35
	v_max_u32_e32 v49, v47, v51
	v_min_u32_e32 v35, v47, v51
	v_max_u32_e32 v44, v50, v52
	v_min_u32_e32 v33, v50, v52
	v_mov_b32_dpp v52, v35 quad_perm:[2,3,0,1] row_mask:0xf bank_mask:0xf bound_ctrl:1
	v_mov_b32_dpp v43, v44 quad_perm:[2,3,0,1] row_mask:0xf bank_mask:0xf bound_ctrl:1
	v_mov_b32_dpp v54, v33 quad_perm:[2,3,0,1] row_mask:0xf bank_mask:0xf bound_ctrl:1
	v_mov_b32_dpp v38, v49 quad_perm:[2,3,0,1] row_mask:0xf bank_mask:0xf bound_ctrl:1
	v_mov_b32_dpp v55, v32 quad_perm:[2,3,0,1] row_mask:0xf bank_mask:0xf bound_ctrl:1
	v_mov_b32_dpp v45, v42 quad_perm:[2,3,0,1] row_mask:0xf bank_mask:0xf bound_ctrl:1
	v_mov_b32_dpp v53, v34 quad_perm:[2,3,0,1] row_mask:0xf bank_mask:0xf bound_ctrl:1
	v_mov_b32_dpp v39, v48 quad_perm:[2,3,0,1] row_mask:0xf bank_mask:0xf bound_ctrl:1
	v_mov_b32_dpp v58, v29 quad_perm:[2,3,0,1] row_mask:0xf bank_mask:0xf bound_ctrl:1
	v_mov_b32_dpp v50, v37 quad_perm:[2,3,0,1] row_mask:0xf bank_mask:0xf bound_ctrl:1
	v_mov_b32_dpp v56, v31 quad_perm:[2,3,0,1] row_mask:0xf bank_mask:0xf bound_ctrl:1
	v_mov_b32_dpp v46, v41 quad_perm:[2,3,0,1] row_mask:0xf bank_mask:0xf bound_ctrl:1
	v_mov_b32_dpp v59, v28 quad_perm:[2,3,0,1] row_mask:0xf bank_mask:0xf bound_ctrl:1
	v_mov_b32_dpp v51, v36 quad_perm:[2,3,0,1] row_mask:0xf bank_mask:0xf bound_ctrl:1
	v_mov_b32_dpp v57, v30 quad_perm:[2,3,0,1] row_mask:0xf bank_mask:0xf bound_ctrl:1
	v_mov_b32_dpp v47, v40 quad_perm:[2,3,0,1] row_mask:0xf bank_mask:0xf bound_ctrl:1
	s_and_saveexec_b64 s[8:9], s[46:47]
	s_cbranch_execz .LBB0_725
	v_max_u32_e32 v40, v40, v54
	v_max_u32_e32 v48, v48, v58
	v_max_u32_e32 v41, v41, v55
	v_max_u32_e32 v49, v49, v59
	v_max_u32_e32 v36, v36, v52
	v_max_u32_e32 v42, v42, v56
	v_max_u32_e32 v37, v37, v53
	v_max_u32_e32 v44, v44, v57
	v_max_u32_e32 v43, v30, v43
	v_max_u32_e32 v50, v34, v50
	v_max_u32_e32 v45, v31, v45
	v_max_u32_e32 v51, v35, v51
	v_max_u32_e32 v38, v28, v38
	v_max_u32_e32 v46, v32, v46
	v_max_u32_e32 v39, v29, v39
	v_max_u32_e32 v47, v33, v47
	v_min_u32_e32 v54, v40, v48
	v_min_u32_e32 v55, v41, v49
	v_min_u32_e32 v52, v36, v42
	v_min_u32_e32 v53, v37, v44
	v_min_u32_e32 v34, v43, v50
	v_min_u32_e32 v35, v45, v51
	v_min_u32_e32 v32, v38, v46
	v_min_u32_e32 v33, v39, v47
	v_max_u32_e32 v40, v40, v48
	v_max_u32_e32 v41, v41, v49
	v_max_u32_e32 v42, v36, v42
	v_max_u32_e32 v44, v37, v44
	v_max_u32_e32 v43, v43, v50
	v_max_u32_e32 v45, v45, v51
	v_max_u32_e32 v46, v38, v46
	v_max_u32_e32 v47, v39, v47
	v_min_u32_e32 v48, v40, v41
	v_min_u32_e32 v36, v42, v44
	v_min_u32_e32 v49, v43, v45
	v_max_u32_e32 v40, v40, v41
	v_max_u32_e32 v41, v42, v44
	v_max_u32_e32 v44, v43, v45
	v_max_u32_e32 v45, v46, v47
	v_min_u32_e32 v58, v54, v55
	v_min_u32_e32 v56, v52, v53
	v_min_u32_e32 v59, v34, v35
	v_min_u32_e32 v28, v32, v33
	v_max_u32_e32 v54, v54, v55
	v_max_u32_e32 v52, v52, v53
	v_max_u32_e32 v55, v34, v35
	v_max_u32_e32 v32, v32, v33
	v_min_u32_e32 v50, v46, v47
	v_min_u32_e32 v42, v40, v41
	v_min_u32_e32 v46, v44, v45
	v_max_u32_e32 v40, v40, v41
	v_max_u32_e32 v44, v44, v45
	v_min_u32_e32 v57, v58, v56
	v_min_u32_e32 v29, v59, v28
	v_max_u32_e32 v56, v58, v56
	v_max_u32_e32 v28, v59, v28
	v_min_u32_e32 v53, v54, v52
	v_min_u32_e32 v33, v55, v32
	v_max_u32_e32 v52, v54, v52
	v_max_u32_e32 v32, v55, v32
	v_min_u32_e32 v37, v48, v36
	v_min_u32_e32 v38, v49, v50
	v_max_u32_e32 v36, v48, v36
	v_max_u32_e32 v48, v49, v50
	v_min_u32_e32 v43, v42, v46
	v_max_u32_e32 v42, v42, v46
	v_min_u32_e32 v41, v40, v44
	v_max_u32_e32 v40, v40, v44
	v_min_u32_e32 v31, v57, v29
	v_max_u32_e32 v30, v57, v29
	v_min_u32_e32 v29, v56, v28
	v_max_u32_e32 v28, v56, v28
	v_min_u32_e32 v35, v53, v33
	v_max_u32_e32 v34, v53, v33
	v_min_u32_e32 v33, v52, v32
	v_max_u32_e32 v32, v52, v32
	v_min_u32_e32 v39, v37, v38
	v_max_u32_e32 v38, v37, v38
	v_min_u32_e32 v37, v36, v48
	v_max_u32_e32 v36, v36, v48
	ds_write_b128 v246, v[40:43]
	ds_write_b128 v246, v[36:39] offset:16
	ds_write_b128 v246, v[32:35] offset:32
	ds_write_b128 v246, v[28:31] offset:48
